# lever 8: mixer-A attention loop issues the bias-table LDS reads of all four heads at the top of the step (QK MFMAs take them as C operand), hiding three exposed LDS round trips per step
# speedup vs baseline: 1.0132x; 1.0032x over previous
.LBB0_806:
	s_min_u32 s8, s7, 8
	s_add_i32 s8, s8, s6
	v_med3_i32 v5, s8, 0, v184
	v_lshl_or_b32 v2, v5, 11, v160
	v_lshl_add_u64 v[94:95], v[172:173], 0, v[2:3]
	v_lshlrev_b32_e32 v2, 12, v5
	v_lshl_add_u64 v[122:123], v[174:175], 0, v[2:3]
	global_load_dwordx4 v[90:93], v[94:95], off
	s_nop 0
	global_load_dwordx4 v[94:97], v[94:95], off offset:1024
	s_nop 0
	global_load_dwordx4 v[106:109], v[122:123], off
	global_load_dwordx4 v[110:113], v[122:123], off offset:1024
	global_load_dwordx4 v[118:121], v[122:123], off offset:2048
	s_nop 0
	global_load_dwordx4 v[122:125], v[122:123], off offset:3072
	s_add_i32 s8, s6, s7
	s_add_i32 s8, s8, -1
	s_cmpk_gt_u32 s8, 0xff
	s_cbranch_scc1 .LBB0_816
	ds_read2_b32 v[214:215], v190 offset1:1
	ds_read2_b32 v[216:217], v190 offset0:2 offset1:3
	ds_read2_b32 v[218:219], v190 offset0:16 offset1:17
	ds_read2_b32 v[220:221], v190 offset0:18 offset1:19
	v_add_u32_e32 v246, 0x504, v190
	v_add_u32_e32 v247, 0x50c, v190
	ds_read2_b32 v[222:223], v246 offset1:1
	ds_read2_b32 v[224:225], v247 offset1:1
	v_add_u32_e32 v246, 0x544, v190
	v_add_u32_e32 v247, 0x54c, v190
	ds_read2_b32 v[226:227], v246 offset1:1
	ds_read2_b32 v[228:229], v247 offset1:1
	v_add_u32_e32 v246, 0xa08, v190
	v_add_u32_e32 v247, 0xa10, v190
	ds_read2_b32 v[230:231], v246 offset1:1
	ds_read2_b32 v[232:233], v247 offset1:1
	v_add_u32_e32 v246, 0xa48, v190
	v_add_u32_e32 v247, 0xa50, v190
	ds_read2_b32 v[234:235], v246 offset1:1
	ds_read2_b32 v[236:237], v247 offset1:1
	v_add_u32_e32 v246, 0xf0c, v190
	v_add_u32_e32 v247, 0xf14, v190
	ds_read2_b32 v[238:239], v246 offset1:1
	ds_read2_b32 v[240:241], v247 offset1:1
	v_add_u32_e32 v246, 0xf4c, v190
	v_add_u32_e32 v247, 0xf54, v190
	ds_read2_b32 v[242:243], v246 offset1:1
	ds_read2_b32 v[244:245], v247 offset1:1
	s_waitcnt vmcnt(11) lgkmcnt(14)
	v_mfma_f32_16x16x32_fp8_fp8 v[134:137], v[130:131], v[70:71], v[214:217]
	v_mfma_f32_16x16x32_fp8_fp8 v[138:141], v[132:133], v[72:73], v[134:137]
	s_waitcnt vmcnt(10) lgkmcnt(12)
	v_mfma_f32_16x16x32_fp8_fp8 v[134:137], v[126:127], v[70:71], v[218:221]
	v_mfma_f32_16x16x32_fp8_fp8 v[134:137], v[128:129], v[72:73], v[134:137]
	s_nop 4
	v_max_f32_e32 v2, v139, v139
	v_max_f32_e32 v5, v138, v138
	v_max_f32_e32 v2, v5, v2
	v_max_f32_e32 v5, v141, v141
	v_max_f32_e32 v191, v140, v140
	v_max_f32_e32 v5, v191, v5
	v_max_f32_e32 v191, v137, v137
	v_max_f32_e32 v192, v136, v136
	v_max_f32_e32 v191, v192, v191
	v_max3_f32 v191, v134, v135, v191
	v_max3_f32 v2, v2, v5, v191
	v_mov_b32_e32 v5, v2
	s_nop 1
	v_permlane16_swap_b32_e32 v2, v5
	v_max_f32_e32 v5, v5, v5
	v_max_f32_e32 v2, v2, v2
	v_max_f32_e32 v2, v2, v5
	v_mov_b32_e32 v5, v2
	s_nop 1
	v_permlane32_swap_b32_e32 v2, v5
	v_max_f32_e32 v5, v5, v5
	v_max_f32_e32 v2, v2, v2
	v_max_f32_e32 v2, v2, v5
	v_cmp_gt_f32_e32 vcc, v2, v176
	s_cbranch_vccz .LBB0_809
	v_max_f32_e32 v2, v2, v2
	v_max_f32_e32 v5, v176, v176
	v_max_f32_e32 v5, v5, v2
	v_sub_f32_e32 v2, v176, v5
	v_exp_f32_e32 v2, v2
	v_mov_b32_e32 v176, v5
	v_mul_f32_e32 v4, v4, v2
	v_pk_mul_f32 v[68:69], v[68:69], v[2:3] op_sel_hi:[1,0]
	v_pk_mul_f32 v[66:67], v[66:67], v[2:3] op_sel_hi:[1,0]
	v_pk_mul_f32 v[64:65], v[64:65], v[2:3] op_sel_hi:[1,0]
	v_pk_mul_f32 v[62:63], v[62:63], v[2:3] op_sel_hi:[1,0]
	v_pk_mul_f32 v[60:61], v[60:61], v[2:3] op_sel_hi:[1,0]
	v_pk_mul_f32 v[58:59], v[58:59], v[2:3] op_sel_hi:[1,0]
	v_pk_mul_f32 v[56:57], v[56:57], v[2:3] op_sel_hi:[1,0]
	v_pk_mul_f32 v[54:55], v[54:55], v[2:3] op_sel_hi:[1,0]
.LBB0_809:
	v_sub_f32_e32 v134, v134, v176
	v_exp_f32_e32 v193, v134
	v_sub_f32_e32 v134, v135, v176
	v_sub_f32_e32 v2, v138, v176
	v_sub_f32_e32 v138, v140, v176
	v_exp_f32_e32 v194, v134
	v_sub_f32_e32 v134, v136, v176
	v_sub_f32_e32 v5, v139, v176
	v_exp_f32_e32 v191, v138
	v_sub_f32_e32 v138, v141, v176
	v_exp_f32_e32 v195, v134
	v_sub_f32_e32 v134, v137, v176
	v_exp_f32_e32 v2, v2
	v_exp_f32_e32 v5, v5
	v_exp_f32_e32 v192, v138
	v_exp_f32_e32 v196, v134
	v_cvt_pk_bf16_f32 v136, v193, v194
	v_cvt_pk_bf16_f32 v134, v2, v5
	v_cvt_pk_bf16_f32 v135, v191, v192
	v_cvt_pk_bf16_f32 v137, v195, v196
	s_waitcnt vmcnt(9)
	s_nop 0
	v_mfma_f32_16x16x32_bf16 v[66:69], v[114:117], v[134:137], v[66:69]
	s_waitcnt vmcnt(8)
	v_mfma_f32_16x16x32_bf16 v[62:65], v[102:105], v[134:137], v[62:65]
	s_waitcnt vmcnt(7)
	v_mfma_f32_16x16x32_bf16 v[58:61], v[98:101], v[134:137], v[58:61]
	s_waitcnt vmcnt(6)
	v_mfma_f32_16x16x32_bf16 v[54:57], v[86:89], v[134:137], v[54:57]
	s_waitcnt lgkmcnt(0)
	v_mfma_f32_16x16x32_fp8_fp8 v[134:137], v[130:131], v[74:75], v[222:225]
	v_mfma_f32_16x16x32_fp8_fp8 v[138:141], v[132:133], v[76:77], v[134:137]
	v_mfma_f32_16x16x32_fp8_fp8 v[134:137], v[126:127], v[74:75], v[226:229]
	v_mfma_f32_16x16x32_fp8_fp8 v[134:137], v[128:129], v[76:77], v[134:137]
	s_nop 4
	v_max_f32_e32 v197, v139, v139
	v_max_f32_e32 v198, v138, v138
	v_max_f32_e32 v197, v198, v197
	v_max_f32_e32 v198, v141, v141
	v_max_f32_e32 v199, v140, v140
	v_max_f32_e32 v198, v199, v198
	v_max_f32_e32 v199, v137, v137
	v_max_f32_e32 v200, v136, v136
	v_max_f32_e32 v199, v200, v199
	v_max3_f32 v199, v134, v135, v199
	v_max3_f32 v197, v197, v198, v199
	v_mov_b32_e32 v198, v197
	s_nop 1
	v_permlane16_swap_b32_e32 v197, v198
	v_max_f32_e32 v198, v198, v198
	v_max_f32_e32 v197, v197, v197
	v_max_f32_e32 v197, v197, v198
	v_mov_b32_e32 v198, v197
	s_nop 1
	v_permlane32_swap_b32_e32 v197, v198
	v_max_f32_e32 v198, v198, v198
	v_max_f32_e32 v197, v197, v197
	v_max_f32_e32 v197, v197, v198
	v_cmp_gt_f32_e32 vcc, v197, v177
	s_cbranch_vccz .LBB0_811
	v_max_f32_e32 v197, v197, v197
	v_max_f32_e32 v198, v177, v177
	v_max_f32_e32 v197, v198, v197
	v_sub_f32_e32 v177, v177, v197
	v_exp_f32_e32 v198, v177
	v_mov_b32_e32 v177, v197
	v_mul_f32_e32 v189, v189, v198
	v_pk_mul_f32 v[52:53], v[52:53], v[198:199] op_sel_hi:[1,0]
	v_pk_mul_f32 v[50:51], v[50:51], v[198:199] op_sel_hi:[1,0]
	v_pk_mul_f32 v[48:49], v[48:49], v[198:199] op_sel_hi:[1,0]
	v_pk_mul_f32 v[46:47], v[46:47], v[198:199] op_sel_hi:[1,0]
	v_pk_mul_f32 v[44:45], v[44:45], v[198:199] op_sel_hi:[1,0]
	v_pk_mul_f32 v[42:43], v[42:43], v[198:199] op_sel_hi:[1,0]
	v_pk_mul_f32 v[40:41], v[40:41], v[198:199] op_sel_hi:[1,0]
	v_pk_mul_f32 v[38:39], v[38:39], v[198:199] op_sel_hi:[1,0]
.LBB0_811:
	v_sub_f32_e32 v138, v138, v177
	v_sub_f32_e32 v134, v134, v177
	v_exp_f32_e32 v197, v138
	v_sub_f32_e32 v138, v139, v177
	v_exp_f32_e32 v201, v134
	v_sub_f32_e32 v134, v135, v177
	v_exp_f32_e32 v198, v138
	v_sub_f32_e32 v138, v140, v177
	v_exp_f32_e32 v202, v134
	v_sub_f32_e32 v134, v136, v177
	v_exp_f32_e32 v199, v138
	v_sub_f32_e32 v138, v141, v177
	v_exp_f32_e32 v203, v134
	v_sub_f32_e32 v134, v137, v177
	v_exp_f32_e32 v200, v138
	v_exp_f32_e32 v204, v134
	v_cvt_pk_bf16_f32 v134, v197, v198
	v_cvt_pk_bf16_f32 v136, v201, v202
	v_cvt_pk_bf16_f32 v135, v199, v200
	v_cvt_pk_bf16_f32 v137, v203, v204
	s_nop 1
	v_mfma_f32_16x16x32_bf16 v[50:53], v[114:117], v[134:137], v[50:53]
	v_mfma_f32_16x16x32_bf16 v[46:49], v[102:105], v[134:137], v[46:49]
	v_mfma_f32_16x16x32_bf16 v[42:45], v[98:101], v[134:137], v[42:45]
	v_mfma_f32_16x16x32_bf16 v[38:41], v[86:89], v[134:137], v[38:41]
	v_mfma_f32_16x16x32_fp8_fp8 v[134:137], v[130:131], v[78:79], v[230:233]
	v_mfma_f32_16x16x32_fp8_fp8 v[138:141], v[132:133], v[80:81], v[134:137]
	v_mfma_f32_16x16x32_fp8_fp8 v[134:137], v[126:127], v[78:79], v[234:237]
	v_mfma_f32_16x16x32_fp8_fp8 v[134:137], v[128:129], v[80:81], v[134:137]
	s_nop 4
	v_max_f32_e32 v205, v139, v139
	v_max_f32_e32 v206, v138, v138
	v_max_f32_e32 v205, v206, v205
	v_max_f32_e32 v206, v141, v141
	v_max_f32_e32 v207, v140, v140
	v_max_f32_e32 v206, v207, v206
	v_max_f32_e32 v207, v137, v137
	v_max_f32_e32 v208, v136, v136
	v_max_f32_e32 v207, v208, v207
	v_max3_f32 v207, v134, v135, v207
	v_max3_f32 v205, v205, v206, v207
	v_mov_b32_e32 v206, v205
	s_nop 1
	v_permlane16_swap_b32_e32 v205, v206
	v_max_f32_e32 v206, v206, v206
	v_max_f32_e32 v205, v205, v205
	v_max_f32_e32 v205, v205, v206
	v_mov_b32_e32 v206, v205
	s_nop 1
	v_permlane32_swap_b32_e32 v205, v206
	v_max_f32_e32 v206, v206, v206
	v_max_f32_e32 v205, v205, v205
	v_max_f32_e32 v205, v205, v206
	v_cmp_gt_f32_e32 vcc, v205, v178
	s_cbranch_vccz .LBB0_813
	v_max_f32_e32 v205, v205, v205
	v_max_f32_e32 v206, v178, v178
	v_max_f32_e32 v205, v206, v205
	v_sub_f32_e32 v178, v178, v205
	v_exp_f32_e32 v178, v178
	s_nop 0
	v_mul_f32_e32 v188, v188, v178
	v_pk_mul_f32 v[36:37], v[36:37], v[178:179] op_sel_hi:[1,0]
	v_pk_mul_f32 v[34:35], v[34:35], v[178:179] op_sel_hi:[1,0]
	v_pk_mul_f32 v[32:33], v[32:33], v[178:179] op_sel_hi:[1,0]
	v_pk_mul_f32 v[30:31], v[30:31], v[178:179] op_sel_hi:[1,0]
	v_pk_mul_f32 v[28:29], v[28:29], v[178:179] op_sel_hi:[1,0]
	v_pk_mul_f32 v[26:27], v[26:27], v[178:179] op_sel_hi:[1,0]
	v_pk_mul_f32 v[24:25], v[24:25], v[178:179] op_sel_hi:[1,0]
	v_pk_mul_f32 v[22:23], v[22:23], v[178:179] op_sel_hi:[1,0]
	v_mov_b32_e32 v178, v205
.LBB0_813:
	v_sub_f32_e32 v138, v138, v178
	v_sub_f32_e32 v139, v139, v178
	v_sub_f32_e32 v140, v140, v178
	v_sub_f32_e32 v141, v141, v178
	v_sub_f32_e32 v134, v134, v178
	v_sub_f32_e32 v135, v135, v178
	v_sub_f32_e32 v136, v136, v178
	v_sub_f32_e32 v137, v137, v178
	v_exp_f32_e32 v138, v138
	v_exp_f32_e32 v139, v139
	v_exp_f32_e32 v140, v140
	v_exp_f32_e32 v141, v141
	v_exp_f32_e32 v134, v134
	v_exp_f32_e32 v135, v135
	v_exp_f32_e32 v136, v136
	v_exp_f32_e32 v137, v137
	v_cvt_pk_bf16_f32 v206, v138, v139
	v_cvt_pk_bf16_f32 v207, v140, v141
	v_cvt_pk_bf16_f32 v208, v134, v135
	v_cvt_pk_bf16_f32 v209, v136, v137
	s_nop 1
	v_mfma_f32_16x16x32_bf16 v[34:37], v[114:117], v[206:209], v[34:37]
	v_mfma_f32_16x16x32_bf16 v[30:33], v[102:105], v[206:209], v[30:33]
	v_mfma_f32_16x16x32_bf16 v[26:29], v[98:101], v[206:209], v[26:29]
	v_mfma_f32_16x16x32_bf16 v[22:25], v[86:89], v[206:209], v[22:25]
	v_mfma_f32_16x16x32_fp8_fp8 v[206:209], v[130:131], v[82:83], v[238:241]
	v_mfma_f32_16x16x32_fp8_fp8 v[210:213], v[126:127], v[82:83], v[242:245]
	v_mfma_f32_16x16x32_fp8_fp8 v[130:133], v[132:133], v[84:85], v[206:209]
	v_mfma_f32_16x16x32_fp8_fp8 v[126:129], v[128:129], v[84:85], v[210:213]
	s_nop 6
	v_max_f32_e32 v205, v131, v131
	v_max_f32_e32 v206, v130, v130
	v_max_f32_e32 v207, v133, v133
	v_max_f32_e32 v205, v206, v205
	v_max_f32_e32 v206, v132, v132
	v_max_f32_e32 v206, v206, v207
	v_max_f32_e32 v207, v129, v129
	v_max_f32_e32 v208, v128, v128
	v_max_f32_e32 v207, v208, v207
	v_max3_f32 v207, v126, v127, v207
	v_max3_f32 v205, v205, v206, v207
	v_mov_b32_e32 v206, v205
	s_nop 1
	v_permlane16_swap_b32_e32 v205, v206
	v_max_f32_e32 v206, v206, v206
	v_max_f32_e32 v205, v205, v205
	v_max_f32_e32 v205, v205, v206
	v_mov_b32_e32 v206, v205
	s_nop 1
	v_permlane32_swap_b32_e32 v205, v206
	v_max_f32_e32 v206, v206, v206
	v_max_f32_e32 v205, v205, v205
	v_max_f32_e32 v205, v205, v206
	v_cmp_gt_f32_e32 vcc, v205, v179
	s_cbranch_vccz .LBB0_815
	v_max_f32_e32 v205, v205, v205
	v_max_f32_e32 v206, v179, v179
	v_max_f32_e32 v205, v206, v205
	v_sub_f32_e32 v179, v179, v205
	v_exp_f32_e32 v206, v179
	v_mov_b32_e32 v179, v205
	v_mul_f32_e32 v187, v187, v206
	v_pk_mul_f32 v[20:21], v[20:21], v[206:207] op_sel_hi:[1,0]
	v_pk_mul_f32 v[18:19], v[18:19], v[206:207] op_sel_hi:[1,0]
	v_pk_mul_f32 v[16:17], v[16:17], v[206:207] op_sel_hi:[1,0]
	v_pk_mul_f32 v[14:15], v[14:15], v[206:207] op_sel_hi:[1,0]
	v_pk_mul_f32 v[12:13], v[12:13], v[206:207] op_sel_hi:[1,0]
	v_pk_mul_f32 v[10:11], v[10:11], v[206:207] op_sel_hi:[1,0]
	v_pk_mul_f32 v[8:9], v[8:9], v[206:207] op_sel_hi:[1,0]
	v_pk_mul_f32 v[6:7], v[6:7], v[206:207] op_sel_hi:[1,0]
